# attention K/V key tiles prefetched three tiles ahead through three register sets with counted vmcnt waits (was one tile ahead)
# baseline (speedup 1.0000x reference)
.LBB0_810:
	s_and_b64 vcc, exec, s[6:7]
	s_cbranch_vccz .LBB0_795
	s_bfe_u32 s11, s10, 0x20005
	s_lshl_b32 s20, s11, 2
	s_add_i32 s20, s20, s13
	s_ashr_i32 s8, s10, 7
	s_and_b32 s10, s10, 31
	s_lshl_b32 s6, s20, 6
	v_mov_b32_e32 v38, v182
	s_lshl_b32 s9, s10, 7
	s_ashr_i32 s7, s6, 31
	s_lshl_b32 s18, s8, 12
	v_ashrrev_i32_e32 v165, 5, v38
	s_or_b32 s19, s9, s17
	s_lshl_b64 s[6:7], s[6:7], 1
	v_and_b32_e32 v184, 31, v38
	s_add_u32 s28, s94, s6
	v_lshlrev_b32_e32 v170, 3, v165
	v_or_b32_e32 v39, s19, v184
	s_addc_u32 s29, s95, s7
	v_ashrrev_i32_e32 v171, 31, v170
	v_lshl_add_u64 v[26:27], v[170:171], 1, s[28:29]
	v_or_b32_e32 v2, s18, v39
	v_mad_i64_i32 v[2:3], s[28:29], v2, s30, v[26:27]
	global_load_dwordx4 v[28:31], v[2:3], off
	s_waitcnt lgkmcnt(0)
	global_load_dwordx4 v[32:35], v[2:3], off offset:32
	global_load_dwordx4 v[6:9], v[2:3], off offset:64
	s_nop 0
	global_load_dwordx4 v[2:5], v[2:3], off offset:96
	v_cvt_f32_i32_e32 v10, v170
	s_lshr_b32 s21, s19, 6
	v_cvt_f32_ubyte0_e32 v23, s21
	v_cvt_f32_ubyte0_e32 v40, v184
	v_mul_f32_e32 v10, 0xbf549a78, v10
	v_exp_f32_e32 v62, v10
	v_or_b32_e32 v10, 1, v170
	v_cvt_f32_i32_e32 v11, v10
	s_add_i32 s20, s20, s12
	v_mul_f32_e32 v36, v62, v40
	v_mul_f32_e32 v37, 0.15915494, v36
	v_mul_f32_e32 v11, 0xbf549a78, v11
	v_exp_f32_e32 v63, v11
	v_or_b32_e32 v11, 2, v170
	v_cvt_f32_i32_e32 v13, v11
	v_sin_f32_e32 v36, v37
	v_mul_f32_e32 v11, v63, v23
	v_mul_f32_e32 v14, 0.15915494, v11
	v_mul_f32_e32 v13, 0xbf549a78, v13
	v_sin_f32_e32 v11, v14
	v_exp_f32_e32 v64, v13
	v_cos_f32_e32 v13, v14
	v_or_b32_e32 v14, 3, v170
	v_cvt_f32_i32_e32 v15, v14
	v_cos_f32_e32 v48, v37
	v_mul_f32_e32 v37, v63, v40
	v_mul_f32_e32 v41, 0.15915494, v37
	v_mul_f32_e32 v15, 0xbf549a78, v15
	v_exp_f32_e32 v65, v15
	v_or_b32_e32 v15, 4, v170
	v_cvt_f32_i32_e32 v17, v15
	v_sin_f32_e32 v37, v41
	v_mul_f32_e32 v15, v65, v23
	v_mul_f32_e32 v18, 0.15915494, v15
	v_mul_f32_e32 v17, 0xbf549a78, v17
	v_sin_f32_e32 v15, v18
	v_exp_f32_e32 v66, v17
	v_cos_f32_e32 v17, v18
	v_or_b32_e32 v18, 5, v170
	v_cvt_f32_i32_e32 v19, v18
	v_cos_f32_e32 v49, v41
	v_mul_f32_e32 v41, v64, v40
	v_mul_f32_e32 v41, 0.15915494, v41
	v_mul_f32_e32 v19, 0xbf549a78, v19
	v_exp_f32_e32 v67, v19
	v_or_b32_e32 v19, 6, v170
	v_cvt_f32_i32_e32 v19, v19
	v_sin_f32_e32 v50, v41
	v_cos_f32_e32 v52, v41
	v_mul_f32_e32 v41, v65, v40
	v_mul_f32_e32 v19, 0xbf549a78, v19
	v_exp_f32_e32 v68, v19
	v_or_b32_e32 v19, 7, v170
	v_cvt_f32_i32_e32 v22, v19
	v_mul_f32_e32 v41, 0.15915494, v41
	v_mul_f32_e32 v10, v62, v23
	v_sin_f32_e32 v51, v41
	v_mul_f32_e32 v22, 0xbf549a78, v22
	v_exp_f32_e32 v69, v22
	v_cos_f32_e32 v53, v41
	v_mul_f32_e32 v41, v66, v40
	v_mul_f32_e32 v12, 0.15915494, v10
	v_mul_f32_e32 v41, 0.15915494, v41
	v_sin_f32_e32 v10, v12
	v_cos_f32_e32 v12, v12
	v_sin_f32_e32 v54, v41
	v_cos_f32_e32 v56, v41
	v_mul_f32_e32 v41, v67, v40
	v_mul_f32_e32 v41, 0.15915494, v41
	v_mul_f32_e32 v14, v64, v23
	v_sin_f32_e32 v55, v41
	v_cos_f32_e32 v57, v41
	v_mul_f32_e32 v41, v68, v40
	v_mul_f32_e32 v40, v69, v40
	v_mul_f32_e32 v16, 0.15915494, v14
	v_mul_f32_e32 v41, 0.15915494, v41
	v_mul_f32_e32 v40, 0.15915494, v40
	s_waitcnt vmcnt(2)
	v_lshlrev_b32_e32 v42, 16, v32
	v_and_b32_e32 v43, 0xffff0000, v32
	v_sin_f32_e32 v14, v16
	v_cos_f32_e32 v16, v16
	v_sin_f32_e32 v58, v41
	v_cos_f32_e32 v60, v41
	v_sin_f32_e32 v59, v40
	v_cos_f32_e32 v61, v40
	v_lshlrev_b32_e32 v40, 16, v28
	v_and_b32_e32 v41, 0xffff0000, v28
	v_pk_mul_f32 v[44:45], v[12:13], v[42:43]
	v_pk_mul_f32 v[42:43], v[10:11], v[42:43]
	v_pk_fma_f32 v[44:45], v[10:11], v[40:41], v[44:45]
	v_pk_fma_f32 v[40:41], v[12:13], v[40:41], v[42:43] neg_lo:[0,0,1] neg_hi:[0,0,1]
	v_mul_f32_e32 v18, v66, v23
	v_mul_f32_e32 v21, v67, v23
	v_pk_mul_f32 v[40:41], v[40:41], s[84:85] op_sel_hi:[1,0]
	v_mul_f32_e32 v20, 0.15915494, v18
	v_mul_f32_e32 v21, 0.15915494, v21
	v_cvt_pk_bf16_f32 v100, v40, v41
	v_pk_mul_f32 v[40:41], v[44:45], s[84:85] op_sel_hi:[1,0]
	v_lshlrev_b32_e32 v32, 16, v33
	v_and_b32_e32 v33, 0xffff0000, v33
	v_sin_f32_e32 v18, v20
	v_cos_f32_e32 v20, v20
	v_sin_f32_e32 v19, v21
	v_cos_f32_e32 v21, v21
	v_cvt_pk_bf16_f32 v104, v40, v41
	v_lshlrev_b32_e32 v28, 16, v29
	v_and_b32_e32 v29, 0xffff0000, v29
	v_pk_mul_f32 v[40:41], v[16:17], v[32:33]
	v_pk_mul_f32 v[32:33], v[14:15], v[32:33]
	v_pk_fma_f32 v[40:41], v[14:15], v[28:29], v[40:41]
	v_pk_fma_f32 v[28:29], v[16:17], v[28:29], v[32:33] neg_lo:[0,0,1] neg_hi:[0,0,1]
	v_mul_f32_e32 v24, v68, v23
	v_pk_mul_f32 v[28:29], v[28:29], s[84:85] op_sel_hi:[1,0]
	v_mul_f32_e32 v23, v69, v23
	v_cvt_pk_bf16_f32 v101, v28, v29
	v_pk_mul_f32 v[28:29], v[40:41], s[84:85] op_sel_hi:[1,0]
	v_lshlrev_b32_e32 v32, 16, v34
	v_and_b32_e32 v33, 0xffff0000, v34
	v_mul_f32_e32 v24, 0.15915494, v24
	v_mul_f32_e32 v25, 0.15915494, v23
	v_cvt_pk_bf16_f32 v105, v28, v29
	v_lshlrev_b32_e32 v28, 16, v30
	v_and_b32_e32 v29, 0xffff0000, v30
	v_pk_mul_f32 v[40:41], v[20:21], v[32:33]
	v_pk_mul_f32 v[32:33], v[18:19], v[32:33]
	v_sin_f32_e32 v22, v24
	v_cos_f32_e32 v24, v24
	v_sin_f32_e32 v23, v25
	v_cos_f32_e32 v25, v25
	v_pk_fma_f32 v[40:41], v[18:19], v[28:29], v[40:41]
	v_pk_fma_f32 v[28:29], v[20:21], v[28:29], v[32:33] neg_lo:[0,0,1] neg_hi:[0,0,1]
	v_lshlrev_b32_e32 v30, 16, v35
	v_pk_mul_f32 v[28:29], v[28:29], s[84:85] op_sel_hi:[1,0]
	s_ashr_i32 s21, s20, 31
	v_cvt_pk_bf16_f32 v102, v28, v29
	v_pk_mul_f32 v[28:29], v[40:41], s[84:85] op_sel_hi:[1,0]
	s_lshl_b64 s[20:21], s[20:21], 2
	v_cvt_pk_bf16_f32 v106, v28, v29
	v_lshlrev_b32_e32 v28, 16, v31
	v_and_b32_e32 v29, 0xffff0000, v31
	v_and_b32_e32 v31, 0xffff0000, v35
	v_pk_mul_f32 v[32:33], v[24:25], v[30:31]
	v_pk_mul_f32 v[30:31], v[22:23], v[30:31]
	v_pk_fma_f32 v[32:33], v[22:23], v[28:29], v[32:33]
	v_pk_fma_f32 v[28:29], v[24:25], v[28:29], v[30:31] neg_lo:[0,0,1] neg_hi:[0,0,1]
	s_waitcnt vmcnt(0)
	v_lshlrev_b32_e32 v30, 16, v2
	v_and_b32_e32 v31, 0xffff0000, v2
	v_or_b32_e32 v2, 32, v39
	v_or_b32_e32 v2, s18, v2
	v_pk_mul_f32 v[28:29], v[28:29], s[84:85] op_sel_hi:[1,0]
	v_mad_i64_i32 v[26:27], s[28:29], v2, s30, v[26:27]
	v_cvt_pk_bf16_f32 v103, v28, v29
	v_pk_mul_f32 v[28:29], v[32:33], s[84:85] op_sel_hi:[1,0]
	global_load_dwordx4 v[40:43], v[26:27], off
	global_load_dwordx4 v[44:47], v[26:27], off offset:32
	v_cvt_pk_bf16_f32 v107, v28, v29
	v_lshlrev_b32_e32 v28, 16, v6
	v_and_b32_e32 v29, 0xffff0000, v6
	v_pk_mul_f32 v[32:33], v[48:49], v[30:31]
	v_pk_mul_f32 v[30:31], v[36:37], v[30:31]
	v_pk_fma_f32 v[32:33], v[36:37], v[28:29], v[32:33]
	v_pk_fma_f32 v[28:29], v[48:49], v[28:29], v[30:31] neg_lo:[0,0,1] neg_hi:[0,0,1]
	v_lshlrev_b32_e32 v2, 16, v3
	v_pk_mul_f32 v[28:29], v[28:29], s[84:85] op_sel_hi:[1,0]
	v_and_b32_e32 v3, 0xffff0000, v3
	v_cvt_pk_bf16_f32 v108, v28, v29
	v_pk_mul_f32 v[28:29], v[32:33], s[84:85] op_sel_hi:[1,0]
	v_lshlrev_b32_e32 v6, 16, v7
	v_cvt_pk_bf16_f32 v112, v28, v29
	v_and_b32_e32 v7, 0xffff0000, v7
	v_pk_mul_f32 v[28:29], v[52:53], v[2:3]
	v_pk_mul_f32 v[2:3], v[50:51], v[2:3]
	v_pk_fma_f32 v[28:29], v[50:51], v[6:7], v[28:29]
	v_pk_fma_f32 v[2:3], v[52:53], v[6:7], v[2:3] neg_lo:[0,0,1] neg_hi:[0,0,1]
	v_lshlrev_b32_e32 v6, 16, v4
	v_pk_mul_f32 v[2:3], v[2:3], s[84:85] op_sel_hi:[1,0]
	v_and_b32_e32 v7, 0xffff0000, v4
	v_cvt_pk_bf16_f32 v109, v2, v3
	v_pk_mul_f32 v[2:3], v[28:29], s[84:85] op_sel_hi:[1,0]
	v_pk_mul_f32 v[28:29], v[56:57], v[6:7]
	v_cvt_pk_bf16_f32 v113, v2, v3
	v_lshlrev_b32_e32 v2, 16, v8
	v_and_b32_e32 v3, 0xffff0000, v8
	v_pk_mul_f32 v[6:7], v[54:55], v[6:7]
	v_pk_fma_f32 v[28:29], v[54:55], v[2:3], v[28:29]
	v_pk_fma_f32 v[2:3], v[56:57], v[2:3], v[6:7] neg_lo:[0,0,1] neg_hi:[0,0,1]
	v_lshlrev_b32_e32 v4, 16, v5
	v_pk_mul_f32 v[2:3], v[2:3], s[84:85] op_sel_hi:[1,0]
	v_and_b32_e32 v5, 0xffff0000, v5
	v_cvt_pk_bf16_f32 v110, v2, v3
	v_pk_mul_f32 v[2:3], v[28:29], s[84:85] op_sel_hi:[1,0]
	v_pk_mul_f32 v[6:7], v[60:61], v[4:5]
	v_cvt_pk_bf16_f32 v114, v2, v3
	v_lshlrev_b32_e32 v2, 16, v9
	v_and_b32_e32 v3, 0xffff0000, v9
	v_pk_mul_f32 v[4:5], v[58:59], v[4:5]
	v_pk_fma_f32 v[6:7], v[58:59], v[2:3], v[6:7]
	v_pk_fma_f32 v[2:3], v[60:61], v[2:3], v[4:5] neg_lo:[0,0,1] neg_hi:[0,0,1]
	v_cmp_gt_u32_e32 vcc, 32, v38
	v_pk_mul_f32 v[2:3], v[2:3], s[84:85] op_sel_hi:[1,0]
	v_lshlrev_b32_e32 v171, 4, v165
	v_cvt_pk_bf16_f32 v111, v2, v3
	v_pk_mul_f32 v[2:3], v[6:7], s[84:85] op_sel_hi:[1,0]
	v_cndmask_b32_e64 v191, 0, 1.0, vcc
	v_cvt_pk_bf16_f32 v115, v2, v3
	global_load_dwordx4 v[6:9], v[26:27], off offset:64
	global_load_dwordx4 v[2:5], v[26:27], off offset:96
	v_bitop3_b32 v26, v39, 63, 32 bitop3:0xc8
	v_cvt_f32_ubyte0_e32 v27, v26
	s_load_dwordx2 s[28:29], s[0:1], 0x50
	v_mul_f32_e32 v26, v62, v27
	v_mul_f32_e32 v26, 0.15915494, v26
	v_sin_f32_e32 v48, v26
	v_cos_f32_e32 v50, v26
	v_mul_f32_e32 v26, v63, v27
	v_mul_f32_e32 v26, 0.15915494, v26
	v_sin_f32_e32 v49, v26
	v_cos_f32_e32 v51, v26
	s_waitcnt lgkmcnt(0)
	s_add_u32 s20, s28, s20
	s_addc_u32 s21, s29, s21
	s_cmp_eq_u32 s10, 0
	s_cselect_b32 s24, 4, 6
	v_mul_f32_e32 v26, v64, v27
	v_mul_f32_e32 v26, 0.15915494, v26
	v_sin_f32_e32 v34, v26
	v_cos_f32_e32 v36, v26
	v_mul_f32_e32 v26, v65, v27
	v_mul_f32_e32 v26, 0.15915494, v26
	v_sin_f32_e32 v35, v26
	v_cos_f32_e32 v37, v26
	v_mul_f32_e32 v26, v66, v27
	v_mul_f32_e32 v26, 0.15915494, v26
	v_sin_f32_e32 v30, v26
	v_cos_f32_e32 v32, v26
	s_waitcnt vmcnt(3)
	v_lshlrev_b32_e32 v52, 16, v40
	s_waitcnt vmcnt(2)
	v_lshlrev_b32_e32 v54, 16, v44
	v_and_b32_e32 v55, 0xffff0000, v44
	v_and_b32_e32 v53, 0xffff0000, v40
	v_pk_mul_f32 v[56:57], v[12:13], v[54:55]
	v_mul_f32_e32 v26, v67, v27
	v_pk_fma_f32 v[56:57], v[10:11], v[52:53], v[56:57]
	v_pk_mul_f32 v[10:11], v[10:11], v[54:55]
	v_mul_f32_e32 v26, 0.15915494, v26
	v_pk_fma_f32 v[10:11], v[12:13], v[52:53], v[10:11] neg_lo:[0,0,1] neg_hi:[0,0,1]
	v_lshlrev_b32_e32 v12, 16, v45
	v_pk_mul_f32 v[10:11], v[10:11], s[84:85] op_sel_hi:[1,0]
	v_and_b32_e32 v13, 0xffff0000, v45
	v_cvt_pk_bf16_f32 v116, v10, v11
	v_pk_mul_f32 v[10:11], v[56:57], s[84:85] op_sel_hi:[1,0]
	v_sin_f32_e32 v31, v26
	v_cvt_pk_bf16_f32 v120, v10, v11
	v_lshlrev_b32_e32 v10, 16, v41
	v_and_b32_e32 v11, 0xffff0000, v41
	v_pk_mul_f32 v[40:41], v[16:17], v[12:13]
	v_pk_mul_f32 v[12:13], v[14:15], v[12:13]
	v_pk_fma_f32 v[40:41], v[14:15], v[10:11], v[40:41]
	v_pk_fma_f32 v[10:11], v[16:17], v[10:11], v[12:13] neg_lo:[0,0,1] neg_hi:[0,0,1]
	v_lshlrev_b32_e32 v12, 16, v46
	v_pk_mul_f32 v[10:11], v[10:11], s[84:85] op_sel_hi:[1,0]
	v_and_b32_e32 v13, 0xffff0000, v46
	v_cvt_pk_bf16_f32 v117, v10, v11
	v_pk_mul_f32 v[10:11], v[40:41], s[84:85] op_sel_hi:[1,0]
	v_pk_mul_f32 v[14:15], v[20:21], v[12:13]
	v_cvt_pk_bf16_f32 v121, v10, v11
	v_lshlrev_b32_e32 v10, 16, v42
	v_and_b32_e32 v11, 0xffff0000, v42
	v_pk_mul_f32 v[12:13], v[18:19], v[12:13]
	v_pk_fma_f32 v[14:15], v[18:19], v[10:11], v[14:15]
	v_pk_fma_f32 v[10:11], v[20:21], v[10:11], v[12:13] neg_lo:[0,0,1] neg_hi:[0,0,1]
	v_lshlrev_b32_e32 v12, 16, v47
	v_pk_mul_f32 v[10:11], v[10:11], s[84:85] op_sel_hi:[1,0]
	v_and_b32_e32 v13, 0xffff0000, v47
	v_cvt_pk_bf16_f32 v118, v10, v11
	v_pk_mul_f32 v[10:11], v[14:15], s[84:85] op_sel_hi:[1,0]
	v_pk_mul_f32 v[14:15], v[24:25], v[12:13]
	v_cvt_pk_bf16_f32 v122, v10, v11
	v_lshlrev_b32_e32 v10, 16, v43
	v_and_b32_e32 v11, 0xffff0000, v43
	v_pk_mul_f32 v[12:13], v[22:23], v[12:13]
	v_pk_fma_f32 v[14:15], v[22:23], v[10:11], v[14:15]
	v_pk_fma_f32 v[10:11], v[24:25], v[10:11], v[12:13] neg_lo:[0,0,1] neg_hi:[0,0,1]
	global_load_dword v16, v99, s[20:21]
	v_pk_mul_f32 v[10:11], v[10:11], s[84:85] op_sel_hi:[1,0]
	s_cselect_b32 s20, 2, 0
	v_cvt_pk_bf16_f32 v119, v10, v11
	v_pk_mul_f32 v[10:11], v[14:15], s[84:85] op_sel_hi:[1,0]
	s_waitcnt vmcnt(1)
	v_lshlrev_b32_e32 v12, 16, v2
	v_and_b32_e32 v13, 0xffff0000, v2
	s_cmp_eq_u32 s10, 31
	v_cvt_pk_bf16_f32 v123, v10, v11
	v_lshlrev_b32_e32 v10, 16, v6
	v_and_b32_e32 v11, 0xffff0000, v6
	v_pk_mul_f32 v[14:15], v[50:51], v[12:13]
	v_pk_mul_f32 v[12:13], v[48:49], v[12:13]
	s_cselect_b32 s27, -2, 0
	s_lshl_b32 s10, s8, 2
	v_pk_fma_f32 v[14:15], v[48:49], v[10:11], v[14:15]
	v_pk_fma_f32 v[10:11], v[50:51], v[10:11], v[12:13] neg_lo:[0,0,1] neg_hi:[0,0,1]
	s_or_b32 s28, s10, s11
	v_pk_mul_f32 v[10:11], v[10:11], s[84:85] op_sel_hi:[1,0]
	s_ashr_i32 s29, s28, 31
	v_cvt_pk_bf16_f32 v124, v10, v11
	v_pk_mul_f32 v[10:11], v[14:15], s[84:85] op_sel_hi:[1,0]
	s_lshl_b64 s[28:29], s[28:29], 6
	v_cvt_pk_bf16_f32 v128, v10, v11
	v_lshl_add_u64 v[10:11], s[28:29], 0, v[160:161]
	v_readlane_b32 s28, v253, 20
	v_lshlrev_b64 v[12:13], 13, v[10:11]
	v_readlane_b32 s29, v253, 21
	v_add_u32_e32 v17, s18, v160
	s_lshl_b32 s68, s11, 7
	v_lshl_add_u64 v[172:173], s[28:29], 0, v[12:13]
	v_mov_b64_e32 v[12:13], s[94:95]
	v_mad_i64_i32 v[12:13], s[28:29], v17, s30, v[12:13]
	s_add_i32 s21, s9, 0xffffff80
	s_lshl_b32 s31, s20, 6
	v_lshl_add_u64 v[12:13], v[12:13], 0, s[68:69]
	s_add_i32 s10, s31, s21
	v_lshl_add_u64 v[12:13], v[12:13], 0, v[98:99]
	v_mad_i64_i32 v[12:13], s[10:11], s10, v233, v[12:13]
	s_add_i32 s31, s31, s9
	v_lshl_add_u64 v[14:15], v[172:173], 0, v[98:99]
	s_lshl_b32 s10, s31, 1
	s_mov_b32 s11, s69
	v_lshl_add_u64 v[14:15], v[14:15], 0, s[10:11]
	global_load_dwordx4 v[132:135], v[12:13], off offset:2048
	global_load_dwordx4 v[136:139], v[14:15], off offset:-256
	v_lshlrev_b32_e32 v2, 16, v3
	v_and_b32_e32 v3, 0xffff0000, v3
	v_cos_f32_e32 v33, v26
	v_lshlrev_b32_e32 v6, 16, v7
	v_and_b32_e32 v7, 0xffff0000, v7
	v_pk_mul_f32 v[12:13], v[36:37], v[2:3]
	v_pk_mul_f32 v[2:3], v[34:35], v[2:3]
	v_mul_f32_e32 v26, v68, v27
	v_pk_fma_f32 v[2:3], v[36:37], v[6:7], v[2:3] neg_lo:[0,0,1] neg_hi:[0,0,1]
	v_mul_f32_e32 v27, v69, v27
	v_pk_fma_f32 v[12:13], v[34:35], v[6:7], v[12:13]
	v_pk_mul_f32 v[2:3], v[2:3], s[84:85] op_sel_hi:[1,0]
	v_mul_f32_e32 v28, 0.15915494, v26
	v_mul_f32_e32 v29, 0.15915494, v27
	v_cvt_pk_bf16_f32 v125, v2, v3
	v_pk_mul_f32 v[2:3], v[12:13], s[84:85] op_sel_hi:[1,0]
	v_lshlrev_b32_e32 v6, 16, v4
	v_and_b32_e32 v7, 0xffff0000, v4
	v_sin_f32_e32 v26, v28
	v_cos_f32_e32 v28, v28
	v_sin_f32_e32 v27, v29
	v_cos_f32_e32 v29, v29
	v_cvt_pk_bf16_f32 v129, v2, v3
	v_lshlrev_b32_e32 v2, 16, v8
	v_and_b32_e32 v3, 0xffff0000, v8
	v_pk_mul_f32 v[12:13], v[32:33], v[6:7]
	v_pk_mul_f32 v[6:7], v[30:31], v[6:7]
	v_pk_fma_f32 v[12:13], v[30:31], v[2:3], v[12:13]
	v_pk_fma_f32 v[2:3], v[32:33], v[2:3], v[6:7] neg_lo:[0,0,1] neg_hi:[0,0,1]
	v_lshlrev_b32_e32 v4, 16, v5
	v_pk_mul_f32 v[2:3], v[2:3], s[84:85] op_sel_hi:[1,0]
	v_and_b32_e32 v5, 0xffff0000, v5
	v_cvt_pk_bf16_f32 v126, v2, v3
	v_pk_mul_f32 v[2:3], v[12:13], s[84:85] op_sel_hi:[1,0]
	v_pk_mul_f32 v[6:7], v[28:29], v[4:5]
	v_cvt_pk_bf16_f32 v130, v2, v3
	v_lshlrev_b32_e32 v2, 16, v9
	v_and_b32_e32 v3, 0xffff0000, v9
	v_pk_mul_f32 v[4:5], v[26:27], v[4:5]
	v_pk_fma_f32 v[6:7], v[26:27], v[2:3], v[6:7]
	v_pk_fma_f32 v[2:3], v[28:29], v[2:3], v[4:5] neg_lo:[0,0,1] neg_hi:[0,0,1]
	v_mad_i64_i32 v[174:175], s[10:11], v17, s30, 0
	v_pk_mul_f32 v[2:3], v[2:3], s[84:85] op_sel_hi:[1,0]
	s_waitcnt lgkmcnt(0)
	s_barrier
	s_waitcnt vmcnt(2)
	v_mul_f32_e32 v192, 0x3fb8aa3b, v16
	v_cvt_pk_bf16_f32 v127, v2, v3
	v_pk_mul_f32 v[2:3], v[6:7], s[84:85] op_sel_hi:[1,0]
	v_mov_b32_e32 v16, v99
	v_cvt_pk_bf16_f32 v131, v2, v3
	v_lshl_add_u32 v2, s8, 8, v163
	v_mad_i64_i32 v[176:177], s[10:11], v2, s30, 0
	v_readlane_b32 s10, v253, 18
	v_lshlrev_b64 v[2:3], 9, v[10:11]
	v_readlane_b32 s11, v253, 19
	v_mov_b32_e32 v17, v99
	s_add_i32 s24, s27, s24
	v_lshl_add_u64 v[178:179], s[10:11], 0, v[2:3]
	v_lshlrev_b32_e32 v2, 2, v165
	v_sub_u32_e32 v2, v2, v39
	v_add_u32_e32 v185, 0xffffff7f, v2
	v_mov_b32_e32 v2, v99
	v_mov_b32_e32 v3, v99
	v_mov_b32_e32 v4, v99
	v_mov_b32_e32 v5, v99
	v_mov_b32_e32 v6, v99
	v_mov_b32_e32 v7, v99
	v_mov_b32_e32 v8, v99
	v_mov_b32_e32 v9, v99
	v_mov_b32_e32 v10, v99
	v_mov_b32_e32 v11, v99
	v_mov_b32_e32 v12, v99
	v_mov_b32_e32 v13, v99
	v_mov_b32_e32 v14, v99
	v_mov_b32_e32 v15, v99
	v_mov_b64_e32 v[32:33], v[16:17]
	v_mov_b64_e32 v[48:49], v[16:17]
	v_mov_b64_e32 v[64:65], v[16:17]
	s_mov_b32 s31, 0
	s_add_i32 s27, s24, 4
	s_sub_i32 s28, s9, 64
	s_add_i32 s29, s19, 0xffffff41
	s_add_i32 s46, s19, 0xbf
	v_mul_u32_u24_e32 v186, 0x88, v184
	v_lshl_add_u64 v[180:181], v[168:169], 0, s[68:69]
	v_mov_b32_e32 v194, v192
	v_mov_b32_e32 v193, v191
	v_mov_b64_e32 v[30:31], v[14:15]
	v_mov_b64_e32 v[28:29], v[12:13]
	v_mov_b64_e32 v[26:27], v[10:11]
	v_mov_b64_e32 v[24:25], v[8:9]
	v_mov_b64_e32 v[22:23], v[6:7]
	v_mov_b64_e32 v[20:21], v[4:5]
	v_mov_b64_e32 v[18:19], v[2:3]
	v_mov_b64_e32 v[46:47], v[14:15]
	v_mov_b64_e32 v[44:45], v[12:13]
	v_mov_b64_e32 v[42:43], v[10:11]
	v_mov_b64_e32 v[40:41], v[8:9]
	v_mov_b64_e32 v[38:39], v[6:7]
	v_mov_b64_e32 v[36:37], v[4:5]
	v_mov_b64_e32 v[34:35], v[2:3]
	v_mov_b64_e32 v[62:63], v[14:15]
	v_mov_b64_e32 v[60:61], v[12:13]
	v_mov_b64_e32 v[58:59], v[10:11]
	v_mov_b64_e32 v[56:57], v[8:9]
	v_mov_b64_e32 v[54:55], v[6:7]
	v_mov_b64_e32 v[52:53], v[4:5]
	v_mov_b64_e32 v[50:51], v[2:3]
	s_mov_b32 s100, 1
	s_cmp_ge_i32 s100, s24
	s_cbranch_scc1 .Lpf1P1_ctx
	s_add_i32 s42, s100, s20
	s_add_i32 s42, s42, -1
	s_lshl_b32 s42, s42, 6
	s_add_i32 s42, s28, s42
	v_mov_b64_e32 v[66:67], v[172:173]
	v_mov_b64_e32 v[68:69], v[174:175]
	s_branch .Lpf1P1_go
.Lpf1P1_ctx:
	s_sub_i32 s42, s100, s24
	s_lshl_b32 s42, s42, 6
	v_mov_b64_e32 v[66:67], v[178:179]
	v_mov_b64_e32 v[68:69], v[176:177]
.Lpf1P1_go:
	v_lshl_add_u64 v[68:69], v[180:181], 0, v[68:69]
	s_ashr_i32 s43, s42, 31
	v_lshl_add_u64 v[66:67], v[66:67], 0, v[98:99]
	v_mad_i64_i32 v[68:69], s[44:45], s42, v233, v[68:69]
	v_lshl_add_u64 v[66:67], s[42:43], 1, v[66:67]
	global_load_dwordx4 v[212:215], v[68:69], off offset:2048
	global_load_dwordx4 v[216:219], v[66:67], off
	s_mov_b32 s100, 2
	s_cmp_ge_i32 s100, s24
	s_cbranch_scc1 .Lpf1P2_ctx
	s_add_i32 s42, s100, s20
	s_add_i32 s42, s42, -1
	s_lshl_b32 s42, s42, 6
	s_add_i32 s42, s28, s42
	v_mov_b64_e32 v[66:67], v[172:173]
	v_mov_b64_e32 v[68:69], v[174:175]
	s_branch .Lpf1P2_go

.Lpf1P2_go:
	v_lshl_add_u64 v[68:69], v[180:181], 0, v[68:69]
	s_ashr_i32 s43, s42, 31
	v_lshl_add_u64 v[66:67], v[66:67], 0, v[98:99]
	v_mad_i64_i32 v[68:69], s[44:45], s42, v233, v[68:69]
	v_lshl_add_u64 v[66:67], s[42:43], 1, v[66:67]
	global_load_dwordx4 v[240:243], v[68:69], off offset:2048
	global_load_dwordx4 v[226:229], v[66:67], off
	s_mov_b32 s101, 0

.LBB0_816:
	s_bitcmp1_b32 s31, 0
	s_cselect_b32 s42, 0x4600, 0
	s_add_i32 s49, s42, 0
	v_add3_u32 v70, s49, v155, v164
	v_add_u32_e32 v71, s49, v157
	s_add_i32 s47, s31, 1
	v_add3_u32 v71, v71, v164, s89
	s_sub_i32 s42, s27, s31
	s_cmp_gt_i32 s42, 2
	s_cbranch_scc1 .Lpf1_w4
	s_cmp_eq_u32 s42, 2
	s_cbranch_scc1 .Lpf1_w2
	s_waitcnt vmcnt(0)
	s_branch .Lpf1_wd
.Lpf1_w2:
	s_waitcnt vmcnt(2)
	s_branch .Lpf1_wd
.Lpf1_w4:
	s_waitcnt vmcnt(4)
.Lpf1_wd:
	s_cmp_eq_u32 s101, 1
	s_cbranch_scc1 .Lpf1_sB
	s_cmp_eq_u32 s101, 2
	s_cbranch_scc1 .Lpf1_sC
	ds_write_b128 v70, v[132:135]
	ds_write2_b64 v71, v[136:137], v[138:139] offset1:1
	s_branch .Lpf1_sd
.Lpf1_sB:
	ds_write_b128 v70, v[212:215]
	ds_write2_b64 v71, v[216:217], v[218:219] offset1:1
	s_branch .Lpf1_sd
.Lpf1_sC:
	ds_write_b128 v70, v[240:243]
	ds_write2_b64 v71, v[226:227], v[228:229] offset1:1
.Lpf1_sd:
	s_add_i32 s100, s31, 3
	s_cmp_ge_i32 s100, s27
	s_cbranch_scc1 .Lpf1_nl
	s_cmp_ge_i32 s100, s24
	s_cbranch_scc1 .Lpf1L_ctx
	s_add_i32 s42, s100, s20
	s_add_i32 s42, s42, -1
	s_lshl_b32 s42, s42, 6
	s_add_i32 s42, s28, s42
	v_mov_b64_e32 v[66:67], v[172:173]
	v_mov_b64_e32 v[68:69], v[174:175]
	s_branch .Lpf1L_go

.Lpf1L_go:
	v_lshl_add_u64 v[68:69], v[180:181], 0, v[68:69]
	s_ashr_i32 s43, s42, 31
	v_lshl_add_u64 v[66:67], v[66:67], 0, v[98:99]
	v_mad_i64_i32 v[68:69], s[44:45], s42, v233, v[68:69]
	v_lshl_add_u64 v[66:67], s[42:43], 1, v[66:67]
	s_cmp_eq_u32 s101, 1
	s_cbranch_scc1 .Lpf1_lB
	s_cmp_eq_u32 s101, 2
	s_cbranch_scc1 .Lpf1_lC
	global_load_dwordx4 v[132:135], v[68:69], off offset:2048
	global_load_dwordx4 v[136:139], v[66:67], off
	s_branch .Lpf1_nl
.Lpf1_lB:
	global_load_dwordx4 v[212:215], v[68:69], off offset:2048
	global_load_dwordx4 v[216:219], v[66:67], off
	s_branch .Lpf1_nl
.Lpf1_lC:
	global_load_dwordx4 v[240:243], v[68:69], off offset:2048
	global_load_dwordx4 v[226:229], v[66:67], off
.Lpf1_nl:
	s_add_i32 s101, s101, 1
	s_cmp_eq_u32 s101, 3
	s_cselect_b32 s101, 0, s101

.LBB0_854:
	s_and_b64 vcc, exec, s[8:9]
	s_cbranch_vccz .LBB0_839
	s_bfe_u32 s24, s12, 0x20005
	s_lshl_b32 s20, s24, 2
	s_add_i32 s20, s20, s18
	s_and_b32 s21, s12, 31
	s_lshl_b32 s8, s20, 6
	s_ashr_i32 s10, s12, 7
	v_mov_b32_e32 v38, v182
	s_lshl_b32 s11, s21, 7
	s_ashr_i32 s9, s8, 31
	s_lshl_b32 s12, s10, 12
	v_ashrrev_i32_e32 v163, 5, v38
	s_or_b32 s13, s11, s19
	s_lshl_b64 s[8:9], s[8:9], 1
	v_and_b32_e32 v181, 31, v38
	s_add_u32 s28, s94, s8
	v_lshlrev_b32_e32 v168, 3, v163
	v_or_b32_e32 v39, s13, v181
	s_addc_u32 s29, s95, s9
	v_ashrrev_i32_e32 v169, 31, v168
	v_lshl_add_u64 v[26:27], v[168:169], 1, s[28:29]
	v_or_b32_e32 v2, s12, v39
	v_mad_i64_i32 v[2:3], s[28:29], v2, s30, v[26:27]
	global_load_dwordx4 v[28:31], v[2:3], off
	s_waitcnt lgkmcnt(0)
	global_load_dwordx4 v[32:35], v[2:3], off offset:32
	global_load_dwordx4 v[6:9], v[2:3], off offset:64
	s_nop 0
	global_load_dwordx4 v[2:5], v[2:3], off offset:96
	v_cvt_f32_i32_e32 v10, v168
	s_lshr_b32 s27, s13, 6
	v_cvt_f32_ubyte0_e32 v23, s27
	v_cvt_f32_ubyte0_e32 v40, v181
	v_mul_f32_e32 v10, 0xbf549a78, v10
	v_exp_f32_e32 v62, v10
	v_or_b32_e32 v10, 1, v168
	v_cvt_f32_i32_e32 v11, v10
	s_add_i32 s42, s20, s17
	v_mul_f32_e32 v36, v62, v40
	v_mul_f32_e32 v37, 0.15915494, v36
	v_mul_f32_e32 v11, 0xbf549a78, v11
	v_exp_f32_e32 v63, v11
	v_or_b32_e32 v11, 2, v168
	v_cvt_f32_i32_e32 v13, v11
	v_sin_f32_e32 v36, v37
	v_mul_f32_e32 v11, v63, v23
	v_mul_f32_e32 v14, 0.15915494, v11
	v_mul_f32_e32 v13, 0xbf549a78, v13
	v_sin_f32_e32 v11, v14
	v_exp_f32_e32 v64, v13
	v_cos_f32_e32 v13, v14
	v_or_b32_e32 v14, 3, v168
	v_cvt_f32_i32_e32 v15, v14
	v_cos_f32_e32 v48, v37
	v_mul_f32_e32 v37, v63, v40
	v_mul_f32_e32 v41, 0.15915494, v37
	v_mul_f32_e32 v15, 0xbf549a78, v15
	v_exp_f32_e32 v65, v15
	v_or_b32_e32 v15, 4, v168
	v_cvt_f32_i32_e32 v17, v15
	v_sin_f32_e32 v37, v41
	v_mul_f32_e32 v15, v65, v23
	v_mul_f32_e32 v18, 0.15915494, v15
	v_mul_f32_e32 v17, 0xbf549a78, v17
	v_sin_f32_e32 v15, v18
	v_exp_f32_e32 v66, v17
	v_cos_f32_e32 v17, v18
	v_or_b32_e32 v18, 5, v168
	v_cvt_f32_i32_e32 v19, v18
	v_cos_f32_e32 v49, v41
	v_mul_f32_e32 v41, v64, v40
	v_mul_f32_e32 v41, 0.15915494, v41
	v_mul_f32_e32 v19, 0xbf549a78, v19
	v_exp_f32_e32 v67, v19
	v_or_b32_e32 v19, 6, v168
	v_cvt_f32_i32_e32 v19, v19
	v_sin_f32_e32 v50, v41
	v_cos_f32_e32 v52, v41
	v_mul_f32_e32 v41, v65, v40
	v_mul_f32_e32 v19, 0xbf549a78, v19
	v_exp_f32_e32 v68, v19
	v_or_b32_e32 v19, 7, v168
	v_cvt_f32_i32_e32 v22, v19
	v_mul_f32_e32 v41, 0.15915494, v41
	v_mul_f32_e32 v10, v62, v23
	v_sin_f32_e32 v51, v41
	v_mul_f32_e32 v22, 0xbf549a78, v22
	v_exp_f32_e32 v69, v22
	v_cos_f32_e32 v53, v41
	v_mul_f32_e32 v41, v66, v40
	v_mul_f32_e32 v12, 0.15915494, v10
	v_mul_f32_e32 v41, 0.15915494, v41
	v_sin_f32_e32 v10, v12
	v_cos_f32_e32 v12, v12
	v_sin_f32_e32 v54, v41
	v_cos_f32_e32 v56, v41
	v_mul_f32_e32 v41, v67, v40
	v_mul_f32_e32 v41, 0.15915494, v41
	v_mul_f32_e32 v14, v64, v23
	v_sin_f32_e32 v55, v41
	v_cos_f32_e32 v57, v41
	v_mul_f32_e32 v41, v68, v40
	v_mul_f32_e32 v40, v69, v40
	v_mul_f32_e32 v16, 0.15915494, v14
	v_mul_f32_e32 v41, 0.15915494, v41
	v_mul_f32_e32 v40, 0.15915494, v40
	s_waitcnt vmcnt(2)
	v_lshlrev_b32_e32 v42, 16, v32
	v_and_b32_e32 v43, 0xffff0000, v32
	v_sin_f32_e32 v14, v16
	v_cos_f32_e32 v16, v16
	v_sin_f32_e32 v58, v41
	v_cos_f32_e32 v60, v41
	v_sin_f32_e32 v59, v40
	v_cos_f32_e32 v61, v40
	v_lshlrev_b32_e32 v40, 16, v28
	v_and_b32_e32 v41, 0xffff0000, v28
	v_pk_mul_f32 v[44:45], v[12:13], v[42:43]
	v_pk_mul_f32 v[42:43], v[10:11], v[42:43]
	v_pk_fma_f32 v[44:45], v[10:11], v[40:41], v[44:45]
	v_pk_fma_f32 v[40:41], v[12:13], v[40:41], v[42:43] neg_lo:[0,0,1] neg_hi:[0,0,1]
	v_mul_f32_e32 v18, v66, v23
	v_mul_f32_e32 v21, v67, v23
	v_pk_mul_f32 v[40:41], v[40:41], s[84:85] op_sel_hi:[1,0]
	v_mul_f32_e32 v20, 0.15915494, v18
	v_mul_f32_e32 v21, 0.15915494, v21
	v_cvt_pk_bf16_f32 v100, v40, v41
	v_pk_mul_f32 v[40:41], v[44:45], s[84:85] op_sel_hi:[1,0]
	v_lshlrev_b32_e32 v32, 16, v33
	v_and_b32_e32 v33, 0xffff0000, v33
	v_sin_f32_e32 v18, v20
	v_cos_f32_e32 v20, v20
	v_sin_f32_e32 v19, v21
	v_cos_f32_e32 v21, v21
	v_cvt_pk_bf16_f32 v104, v40, v41
	v_lshlrev_b32_e32 v28, 16, v29
	v_and_b32_e32 v29, 0xffff0000, v29
	v_pk_mul_f32 v[40:41], v[16:17], v[32:33]
	v_pk_mul_f32 v[32:33], v[14:15], v[32:33]
	v_pk_fma_f32 v[40:41], v[14:15], v[28:29], v[40:41]
	v_pk_fma_f32 v[28:29], v[16:17], v[28:29], v[32:33] neg_lo:[0,0,1] neg_hi:[0,0,1]
	v_mul_f32_e32 v24, v68, v23
	v_pk_mul_f32 v[28:29], v[28:29], s[84:85] op_sel_hi:[1,0]
	v_mul_f32_e32 v23, v69, v23
	v_cvt_pk_bf16_f32 v101, v28, v29
	v_pk_mul_f32 v[28:29], v[40:41], s[84:85] op_sel_hi:[1,0]
	v_lshlrev_b32_e32 v32, 16, v34
	v_and_b32_e32 v33, 0xffff0000, v34
	v_mul_f32_e32 v24, 0.15915494, v24
	v_mul_f32_e32 v25, 0.15915494, v23
	v_cvt_pk_bf16_f32 v105, v28, v29
	v_lshlrev_b32_e32 v28, 16, v30
	v_and_b32_e32 v29, 0xffff0000, v30
	v_pk_mul_f32 v[40:41], v[20:21], v[32:33]
	v_pk_mul_f32 v[32:33], v[18:19], v[32:33]
	v_sin_f32_e32 v22, v24
	v_cos_f32_e32 v24, v24
	v_sin_f32_e32 v23, v25
	v_cos_f32_e32 v25, v25
	v_pk_fma_f32 v[40:41], v[18:19], v[28:29], v[40:41]
	v_pk_fma_f32 v[28:29], v[20:21], v[28:29], v[32:33] neg_lo:[0,0,1] neg_hi:[0,0,1]
	v_lshlrev_b32_e32 v30, 16, v35
	v_pk_mul_f32 v[28:29], v[28:29], s[84:85] op_sel_hi:[1,0]
	s_ashr_i32 s43, s42, 31
	v_cvt_pk_bf16_f32 v102, v28, v29
	v_pk_mul_f32 v[28:29], v[40:41], s[84:85] op_sel_hi:[1,0]
	s_lshl_b64 s[42:43], s[42:43], 2
	v_cvt_pk_bf16_f32 v106, v28, v29
	v_lshlrev_b32_e32 v28, 16, v31
	v_and_b32_e32 v29, 0xffff0000, v31
	v_and_b32_e32 v31, 0xffff0000, v35
	v_pk_mul_f32 v[32:33], v[24:25], v[30:31]
	v_pk_mul_f32 v[30:31], v[22:23], v[30:31]
	v_pk_fma_f32 v[32:33], v[22:23], v[28:29], v[32:33]
	v_pk_fma_f32 v[28:29], v[24:25], v[28:29], v[30:31] neg_lo:[0,0,1] neg_hi:[0,0,1]
	s_waitcnt vmcnt(0)
	v_lshlrev_b32_e32 v30, 16, v2
	v_and_b32_e32 v31, 0xffff0000, v2
	v_or_b32_e32 v2, 32, v39
	v_or_b32_e32 v2, s12, v2
	v_pk_mul_f32 v[28:29], v[28:29], s[84:85] op_sel_hi:[1,0]
	v_mad_i64_i32 v[26:27], s[28:29], v2, s30, v[26:27]
	v_cvt_pk_bf16_f32 v103, v28, v29
	v_pk_mul_f32 v[28:29], v[32:33], s[84:85] op_sel_hi:[1,0]
	global_load_dwordx4 v[40:43], v[26:27], off
	global_load_dwordx4 v[44:47], v[26:27], off offset:32
	v_cvt_pk_bf16_f32 v107, v28, v29
	v_lshlrev_b32_e32 v28, 16, v6
	v_and_b32_e32 v29, 0xffff0000, v6
	v_pk_mul_f32 v[32:33], v[48:49], v[30:31]
	v_pk_mul_f32 v[30:31], v[36:37], v[30:31]
	v_pk_fma_f32 v[32:33], v[36:37], v[28:29], v[32:33]
	v_pk_fma_f32 v[28:29], v[48:49], v[28:29], v[30:31] neg_lo:[0,0,1] neg_hi:[0,0,1]
	v_lshlrev_b32_e32 v2, 16, v3
	v_pk_mul_f32 v[28:29], v[28:29], s[84:85] op_sel_hi:[1,0]
	v_and_b32_e32 v3, 0xffff0000, v3
	v_cvt_pk_bf16_f32 v108, v28, v29
	v_pk_mul_f32 v[28:29], v[32:33], s[84:85] op_sel_hi:[1,0]
	v_lshlrev_b32_e32 v6, 16, v7
	v_cvt_pk_bf16_f32 v112, v28, v29
	v_and_b32_e32 v7, 0xffff0000, v7
	v_pk_mul_f32 v[28:29], v[52:53], v[2:3]
	v_pk_mul_f32 v[2:3], v[50:51], v[2:3]
	v_pk_fma_f32 v[28:29], v[50:51], v[6:7], v[28:29]
	v_pk_fma_f32 v[2:3], v[52:53], v[6:7], v[2:3] neg_lo:[0,0,1] neg_hi:[0,0,1]
	v_lshlrev_b32_e32 v6, 16, v4
	v_pk_mul_f32 v[2:3], v[2:3], s[84:85] op_sel_hi:[1,0]
	v_and_b32_e32 v7, 0xffff0000, v4
	v_cvt_pk_bf16_f32 v109, v2, v3
	v_pk_mul_f32 v[2:3], v[28:29], s[84:85] op_sel_hi:[1,0]
	v_pk_mul_f32 v[28:29], v[56:57], v[6:7]
	v_cvt_pk_bf16_f32 v113, v2, v3
	v_lshlrev_b32_e32 v2, 16, v8
	v_and_b32_e32 v3, 0xffff0000, v8
	v_pk_mul_f32 v[6:7], v[54:55], v[6:7]
	v_pk_fma_f32 v[28:29], v[54:55], v[2:3], v[28:29]
	v_pk_fma_f32 v[2:3], v[56:57], v[2:3], v[6:7] neg_lo:[0,0,1] neg_hi:[0,0,1]
	v_lshlrev_b32_e32 v4, 16, v5
	v_pk_mul_f32 v[2:3], v[2:3], s[84:85] op_sel_hi:[1,0]
	v_and_b32_e32 v5, 0xffff0000, v5
	v_cvt_pk_bf16_f32 v110, v2, v3
	v_pk_mul_f32 v[2:3], v[28:29], s[84:85] op_sel_hi:[1,0]
	v_pk_mul_f32 v[6:7], v[60:61], v[4:5]
	v_cvt_pk_bf16_f32 v114, v2, v3
	v_lshlrev_b32_e32 v2, 16, v9
	v_and_b32_e32 v3, 0xffff0000, v9
	v_pk_mul_f32 v[4:5], v[58:59], v[4:5]
	v_pk_fma_f32 v[6:7], v[58:59], v[2:3], v[6:7]
	v_pk_fma_f32 v[2:3], v[60:61], v[2:3], v[4:5] neg_lo:[0,0,1] neg_hi:[0,0,1]
	v_cmp_gt_u32_e32 vcc, 32, v38
	v_pk_mul_f32 v[2:3], v[2:3], s[84:85] op_sel_hi:[1,0]
	v_lshlrev_b32_e32 v169, 4, v163
	v_cvt_pk_bf16_f32 v111, v2, v3
	v_pk_mul_f32 v[2:3], v[6:7], s[84:85] op_sel_hi:[1,0]
	v_cndmask_b32_e64 v190, 0, 1.0, vcc
	v_cvt_pk_bf16_f32 v115, v2, v3
	global_load_dwordx4 v[6:9], v[26:27], off offset:64
	global_load_dwordx4 v[2:5], v[26:27], off offset:96
	v_bitop3_b32 v26, v39, 63, 32 bitop3:0xc8
	v_cvt_f32_ubyte0_e32 v27, v26
	s_load_dwordx2 s[28:29], s[0:1], 0x50
	v_mul_f32_e32 v26, v62, v27
	v_mul_f32_e32 v26, 0.15915494, v26
	v_sin_f32_e32 v48, v26
	v_cos_f32_e32 v50, v26
	v_mul_f32_e32 v26, v63, v27
	v_mul_f32_e32 v26, 0.15915494, v26
	v_sin_f32_e32 v49, v26
	v_cos_f32_e32 v51, v26
	s_waitcnt lgkmcnt(0)
	s_add_u32 s28, s28, s42
	s_addc_u32 s29, s29, s43
	s_cmp_eq_u32 s21, 0
	s_cselect_b32 s20, 2, 0
	s_cselect_b32 s27, 4, 6
	s_cmp_eq_u32 s21, 31
	s_cselect_b32 s42, -2, 0
	s_lshl_b32 s21, s10, 2
	s_lshl_b32 s68, s24, 7
	s_lshl_b32 s31, s20, 6
	v_mul_f32_e32 v26, v64, v27
	v_mul_f32_e32 v26, 0.15915494, v26
	v_sin_f32_e32 v34, v26
	v_cos_f32_e32 v36, v26
	v_mul_f32_e32 v26, v65, v27
	v_mul_f32_e32 v26, 0.15915494, v26
	s_waitcnt vmcnt(3)
	v_lshlrev_b32_e32 v52, 16, v40
	s_waitcnt vmcnt(2)
	v_lshlrev_b32_e32 v54, 16, v44
	v_and_b32_e32 v55, 0xffff0000, v44
	v_and_b32_e32 v53, 0xffff0000, v40
	v_pk_mul_f32 v[56:57], v[12:13], v[54:55]
	v_sin_f32_e32 v35, v26
	v_pk_fma_f32 v[56:57], v[10:11], v[52:53], v[56:57]
	v_pk_mul_f32 v[10:11], v[10:11], v[54:55]
	v_cos_f32_e32 v37, v26
	v_pk_fma_f32 v[10:11], v[12:13], v[52:53], v[10:11] neg_lo:[0,0,1] neg_hi:[0,0,1]
	v_lshlrev_b32_e32 v12, 16, v45
	v_pk_mul_f32 v[10:11], v[10:11], s[84:85] op_sel_hi:[1,0]
	v_and_b32_e32 v13, 0xffff0000, v45
	v_cvt_pk_bf16_f32 v116, v10, v11
	v_pk_mul_f32 v[10:11], v[56:57], s[84:85] op_sel_hi:[1,0]
	v_mul_f32_e32 v26, v66, v27
	v_cvt_pk_bf16_f32 v120, v10, v11
	v_lshlrev_b32_e32 v10, 16, v41
	v_and_b32_e32 v11, 0xffff0000, v41
	v_pk_mul_f32 v[40:41], v[16:17], v[12:13]
	v_pk_mul_f32 v[12:13], v[14:15], v[12:13]
	v_pk_fma_f32 v[40:41], v[14:15], v[10:11], v[40:41]
	v_pk_fma_f32 v[10:11], v[16:17], v[10:11], v[12:13] neg_lo:[0,0,1] neg_hi:[0,0,1]
	v_lshlrev_b32_e32 v12, 16, v46
	v_pk_mul_f32 v[10:11], v[10:11], s[84:85] op_sel_hi:[1,0]
	v_and_b32_e32 v13, 0xffff0000, v46
	v_cvt_pk_bf16_f32 v117, v10, v11
	v_pk_mul_f32 v[10:11], v[40:41], s[84:85] op_sel_hi:[1,0]
	v_pk_mul_f32 v[14:15], v[20:21], v[12:13]
	v_cvt_pk_bf16_f32 v121, v10, v11
	v_lshlrev_b32_e32 v10, 16, v42
	v_and_b32_e32 v11, 0xffff0000, v42
	v_pk_mul_f32 v[12:13], v[18:19], v[12:13]
	v_pk_fma_f32 v[14:15], v[18:19], v[10:11], v[14:15]
	v_pk_fma_f32 v[10:11], v[20:21], v[10:11], v[12:13] neg_lo:[0,0,1] neg_hi:[0,0,1]
	v_lshlrev_b32_e32 v12, 16, v47
	v_pk_mul_f32 v[10:11], v[10:11], s[84:85] op_sel_hi:[1,0]
	v_and_b32_e32 v13, 0xffff0000, v47
	v_cvt_pk_bf16_f32 v118, v10, v11
	v_pk_mul_f32 v[10:11], v[14:15], s[84:85] op_sel_hi:[1,0]
	v_pk_mul_f32 v[14:15], v[24:25], v[12:13]
	v_cvt_pk_bf16_f32 v122, v10, v11
	v_lshlrev_b32_e32 v10, 16, v43
	v_and_b32_e32 v11, 0xffff0000, v43
	v_pk_mul_f32 v[12:13], v[22:23], v[12:13]
	v_pk_fma_f32 v[14:15], v[22:23], v[10:11], v[14:15]
	v_pk_fma_f32 v[10:11], v[24:25], v[10:11], v[12:13] neg_lo:[0,0,1] neg_hi:[0,0,1]
	global_load_dword v16, v99, s[28:29]
	v_pk_mul_f32 v[10:11], v[10:11], s[84:85] op_sel_hi:[1,0]
	s_or_b32 s28, s21, s24
	v_cvt_pk_bf16_f32 v119, v10, v11
	v_pk_mul_f32 v[10:11], v[14:15], s[84:85] op_sel_hi:[1,0]
	s_waitcnt vmcnt(1)
	v_lshlrev_b32_e32 v12, 16, v2
	v_and_b32_e32 v13, 0xffff0000, v2
	v_cvt_pk_bf16_f32 v123, v10, v11
	v_lshlrev_b32_e32 v10, 16, v6
	v_and_b32_e32 v11, 0xffff0000, v6
	v_pk_mul_f32 v[14:15], v[50:51], v[12:13]
	v_pk_mul_f32 v[12:13], v[48:49], v[12:13]
	v_pk_fma_f32 v[14:15], v[48:49], v[10:11], v[14:15]
	v_pk_fma_f32 v[10:11], v[50:51], v[10:11], v[12:13] neg_lo:[0,0,1] neg_hi:[0,0,1]
	s_ashr_i32 s29, s28, 31
	v_pk_mul_f32 v[10:11], v[10:11], s[84:85] op_sel_hi:[1,0]
	s_lshl_b64 s[28:29], s[28:29], 6
	v_cvt_pk_bf16_f32 v124, v10, v11
	v_pk_mul_f32 v[10:11], v[14:15], s[84:85] op_sel_hi:[1,0]
	v_add_u32_e32 v17, s12, v160
	v_cvt_pk_bf16_f32 v128, v10, v11
	v_lshl_add_u64 v[10:11], s[28:29], 0, v[160:161]
	v_readlane_b32 s28, v253, 20
	v_lshlrev_b64 v[12:13], 13, v[10:11]
	v_readlane_b32 s29, v253, 21
	s_add_i32 s21, s11, 0xffffff80
	s_add_i32 s43, s31, s21
	v_lshl_add_u64 v[170:171], s[28:29], 0, v[12:13]
	v_mov_b64_e32 v[12:13], s[94:95]
	v_mad_i64_i32 v[12:13], s[28:29], v17, s30, v[12:13]
	v_lshl_add_u64 v[12:13], v[12:13], 0, s[68:69]
	v_lshl_add_u64 v[12:13], v[12:13], 0, v[98:99]
	v_mad_i64_i32 v[12:13], s[28:29], s43, v233, v[12:13]
	s_add_i32 s31, s31, s11
	v_lshl_add_u64 v[14:15], v[170:171], 0, v[98:99]
	s_lshl_b32 s28, s31, 1
	s_mov_b32 s29, s69
	v_lshl_add_u64 v[14:15], v[14:15], 0, s[28:29]
	global_load_dwordx4 v[132:135], v[12:13], off offset:2048
	global_load_dwordx4 v[136:139], v[14:15], off offset:-256
	v_mul_f32_e32 v26, 0.15915494, v26
	v_sin_f32_e32 v30, v26
	v_cos_f32_e32 v32, v26
	v_mul_f32_e32 v26, v67, v27
	v_mul_f32_e32 v26, 0.15915494, v26
	v_lshlrev_b32_e32 v2, 16, v3
	v_and_b32_e32 v3, 0xffff0000, v3
	v_sin_f32_e32 v31, v26
	v_cos_f32_e32 v33, v26
	v_lshlrev_b32_e32 v6, 16, v7
	v_and_b32_e32 v7, 0xffff0000, v7
	v_pk_mul_f32 v[12:13], v[36:37], v[2:3]
	v_pk_mul_f32 v[2:3], v[34:35], v[2:3]
	v_mul_f32_e32 v26, v68, v27
	v_pk_fma_f32 v[2:3], v[36:37], v[6:7], v[2:3] neg_lo:[0,0,1] neg_hi:[0,0,1]
	v_mul_f32_e32 v27, v69, v27
	v_pk_fma_f32 v[12:13], v[34:35], v[6:7], v[12:13]
	v_pk_mul_f32 v[2:3], v[2:3], s[84:85] op_sel_hi:[1,0]
	v_mul_f32_e32 v28, 0.15915494, v26
	v_mul_f32_e32 v29, 0.15915494, v27
	v_cvt_pk_bf16_f32 v125, v2, v3
	v_pk_mul_f32 v[2:3], v[12:13], s[84:85] op_sel_hi:[1,0]
	v_lshlrev_b32_e32 v6, 16, v4
	v_and_b32_e32 v7, 0xffff0000, v4
	v_sin_f32_e32 v26, v28
	v_cos_f32_e32 v28, v28
	v_sin_f32_e32 v27, v29
	v_cos_f32_e32 v29, v29
	v_cvt_pk_bf16_f32 v129, v2, v3
	v_lshlrev_b32_e32 v2, 16, v8
	v_and_b32_e32 v3, 0xffff0000, v8
	v_pk_mul_f32 v[12:13], v[32:33], v[6:7]
	v_pk_mul_f32 v[6:7], v[30:31], v[6:7]
	v_pk_fma_f32 v[12:13], v[30:31], v[2:3], v[12:13]
	v_pk_fma_f32 v[2:3], v[32:33], v[2:3], v[6:7] neg_lo:[0,0,1] neg_hi:[0,0,1]
	v_lshlrev_b32_e32 v4, 16, v5
	v_pk_mul_f32 v[2:3], v[2:3], s[84:85] op_sel_hi:[1,0]
	v_and_b32_e32 v5, 0xffff0000, v5
	v_cvt_pk_bf16_f32 v126, v2, v3
	v_pk_mul_f32 v[2:3], v[12:13], s[84:85] op_sel_hi:[1,0]
	v_pk_mul_f32 v[6:7], v[28:29], v[4:5]
	v_cvt_pk_bf16_f32 v130, v2, v3
	v_lshlrev_b32_e32 v2, 16, v9
	v_and_b32_e32 v3, 0xffff0000, v9
	v_pk_mul_f32 v[4:5], v[26:27], v[4:5]
	v_pk_fma_f32 v[6:7], v[26:27], v[2:3], v[6:7]
	v_pk_fma_f32 v[2:3], v[28:29], v[2:3], v[4:5] neg_lo:[0,0,1] neg_hi:[0,0,1]
	v_mad_i64_i32 v[172:173], s[28:29], v17, s30, 0
	v_pk_mul_f32 v[2:3], v[2:3], s[84:85] op_sel_hi:[1,0]
	s_waitcnt lgkmcnt(0)
	s_barrier
	s_waitcnt vmcnt(2)
	v_mul_f32_e32 v191, 0x3fb8aa3b, v16
	v_cvt_pk_bf16_f32 v127, v2, v3
	v_pk_mul_f32 v[2:3], v[6:7], s[84:85] op_sel_hi:[1,0]
	v_mov_b32_e32 v16, v99
	v_cvt_pk_bf16_f32 v131, v2, v3
	v_lshl_add_u32 v2, s10, 8, v180
	v_mad_i64_i32 v[174:175], s[28:29], v2, s30, 0
	v_readlane_b32 s28, v253, 18
	v_lshlrev_b64 v[2:3], 9, v[10:11]
	v_readlane_b32 s29, v253, 19
	v_mov_b32_e32 v17, v99
	s_add_i32 s24, s42, s27
	v_lshl_add_u64 v[176:177], s[28:29], 0, v[2:3]
	v_lshlrev_b32_e32 v2, 2, v163
	v_sub_u32_e32 v2, v2, v39
	v_add_u32_e32 v184, 0xffffff7f, v2
	v_mov_b32_e32 v2, v99
	v_mov_b32_e32 v3, v99
	v_mov_b32_e32 v4, v99
	v_mov_b32_e32 v5, v99
	v_mov_b32_e32 v6, v99
	v_mov_b32_e32 v7, v99
	v_mov_b32_e32 v8, v99
	v_mov_b32_e32 v9, v99
	v_mov_b32_e32 v10, v99
	v_mov_b32_e32 v11, v99
	v_mov_b32_e32 v12, v99
	v_mov_b32_e32 v13, v99
	v_mov_b32_e32 v14, v99
	v_mov_b32_e32 v15, v99
	v_mov_b64_e32 v[32:33], v[16:17]
	v_mov_b64_e32 v[48:49], v[16:17]
	v_mov_b64_e32 v[64:65], v[16:17]
	s_mov_b32 s31, 0
	s_add_i32 s27, s24, 4
	s_sub_i32 s28, s11, 64
	s_add_i32 s29, s13, 0xffffff41
	s_add_i32 s48, s13, 0xbf
	v_mul_u32_u24_e32 v185, 0x88, v181
	v_lshl_add_u64 v[178:179], v[166:167], 0, s[68:69]
	v_mov_b32_e32 v193, v191
	v_mov_b32_e32 v192, v190
	v_mov_b64_e32 v[30:31], v[14:15]
	v_mov_b64_e32 v[28:29], v[12:13]
	v_mov_b64_e32 v[26:27], v[10:11]
	v_mov_b64_e32 v[24:25], v[8:9]
	v_mov_b64_e32 v[22:23], v[6:7]
	v_mov_b64_e32 v[20:21], v[4:5]
	v_mov_b64_e32 v[18:19], v[2:3]
	v_mov_b64_e32 v[46:47], v[14:15]
	v_mov_b64_e32 v[44:45], v[12:13]
	v_mov_b64_e32 v[42:43], v[10:11]
	v_mov_b64_e32 v[40:41], v[8:9]
	v_mov_b64_e32 v[38:39], v[6:7]
	v_mov_b64_e32 v[36:37], v[4:5]
	v_mov_b64_e32 v[34:35], v[2:3]
	v_mov_b64_e32 v[62:63], v[14:15]
	v_mov_b64_e32 v[60:61], v[12:13]
	v_mov_b64_e32 v[58:59], v[10:11]
	v_mov_b64_e32 v[56:57], v[8:9]
	v_mov_b64_e32 v[54:55], v[6:7]
	v_mov_b64_e32 v[52:53], v[4:5]
	v_mov_b64_e32 v[50:51], v[2:3]
	s_mov_b32 s100, 1
	s_cmp_ge_i32 s100, s24
	s_cbranch_scc1 .Lpf2P1_ctx
	s_add_i32 s42, s100, s20
	s_add_i32 s42, s42, -1
	s_lshl_b32 s42, s42, 6
	s_add_i32 s42, s28, s42
	v_mov_b64_e32 v[66:67], v[170:171]
	v_mov_b64_e32 v[68:69], v[172:173]
	s_branch .Lpf2P1_go
.Lpf2P1_ctx:
	s_sub_i32 s42, s100, s24
	s_lshl_b32 s42, s42, 6
	v_mov_b64_e32 v[66:67], v[176:177]
	v_mov_b64_e32 v[68:69], v[174:175]
.Lpf2P1_go:
	v_lshl_add_u64 v[68:69], v[178:179], 0, v[68:69]
	s_ashr_i32 s43, s42, 31
	v_lshl_add_u64 v[66:67], v[66:67], 0, v[98:99]
	v_mad_i64_i32 v[68:69], s[46:47], s42, v233, v[68:69]
	v_lshl_add_u64 v[66:67], s[42:43], 1, v[66:67]
	global_load_dwordx4 v[212:215], v[68:69], off offset:2048
	global_load_dwordx4 v[216:219], v[66:67], off
	s_mov_b32 s100, 2
	s_cmp_ge_i32 s100, s24
	s_cbranch_scc1 .Lpf2P2_ctx
	s_add_i32 s42, s100, s20
	s_add_i32 s42, s42, -1
	s_lshl_b32 s42, s42, 6
	s_add_i32 s42, s28, s42
	v_mov_b64_e32 v[66:67], v[170:171]
	v_mov_b64_e32 v[68:69], v[172:173]
	s_branch .Lpf2P2_go

.Lpf2P2_go:
	v_lshl_add_u64 v[68:69], v[178:179], 0, v[68:69]
	s_ashr_i32 s43, s42, 31
	v_lshl_add_u64 v[66:67], v[66:67], 0, v[98:99]
	v_mad_i64_i32 v[68:69], s[46:47], s42, v233, v[68:69]
	v_lshl_add_u64 v[66:67], s[42:43], 1, v[66:67]
	global_load_dwordx4 v[240:243], v[68:69], off offset:2048
	global_load_dwordx4 v[226:229], v[66:67], off
	s_mov_b64 s[46:47], s[36:37]
	s_mov_b32 s101, 0

.LBB0_860:
	s_bitcmp1_b32 s31, 0
	s_cselect_b32 s42, 0x4600, 0
	s_add_i32 s51, s42, 0
	v_add3_u32 v70, s51, v155, v162
	v_add_u32_e32 v71, s51, v157
	s_add_i32 s49, s31, 1
	v_add3_u32 v71, v71, v162, s89
	s_sub_i32 s42, s27, s31
	s_cmp_gt_i32 s42, 2
	s_cbranch_scc1 .Lpf2_w4
	s_cmp_eq_u32 s42, 2
	s_cbranch_scc1 .Lpf2_w2
	s_waitcnt vmcnt(0)
	s_branch .Lpf2_wd

.Lpf2_sd:
	s_add_i32 s100, s31, 3
	s_cmp_ge_i32 s100, s27
	s_cbranch_scc1 .Lpf2_nl
	s_cmp_ge_i32 s100, s24
	s_cbranch_scc1 .Lpf2L_ctx
	s_add_i32 s42, s100, s20
	s_add_i32 s42, s42, -1
	s_lshl_b32 s42, s42, 6
	s_add_i32 s42, s28, s42
	v_mov_b64_e32 v[66:67], v[170:171]
	v_mov_b64_e32 v[68:69], v[172:173]
	s_branch .Lpf2L_go

.Lpf2L_go:
	v_lshl_add_u64 v[68:69], v[178:179], 0, v[68:69]
	s_ashr_i32 s43, s42, 31
	v_lshl_add_u64 v[66:67], v[66:67], 0, v[98:99]
	v_mad_i64_i32 v[68:69], s[46:47], s42, v233, v[68:69]
	v_lshl_add_u64 v[66:67], s[42:43], 1, v[66:67]
	s_cmp_eq_u32 s101, 1
	s_cbranch_scc1 .Lpf2_lB
	s_cmp_eq_u32 s101, 2
	s_cbranch_scc1 .Lpf2_lC
	global_load_dwordx4 v[132:135], v[68:69], off offset:2048
	global_load_dwordx4 v[136:139], v[66:67], off
	s_branch .Lpf2_nl

.Lpf2_nl:
	s_mov_b64 s[46:47], s[36:37]
	s_add_i32 s101, s101, 1
	s_cmp_eq_u32 s101, 3
	s_cselect_b32 s101, 0, s101

	.amdhsa_kernel _Z10fwd_kernel4Args
		.amdhsa_group_segment_fixed_size 0
		.amdhsa_private_segment_fixed_size 0
		.amdhsa_kernarg_size 512
		.amdhsa_user_sgpr_count 2
		.amdhsa_user_sgpr_dispatch_ptr 0
		.amdhsa_user_sgpr_queue_ptr 0
		.amdhsa_user_sgpr_kernarg_segment_ptr 1
		.amdhsa_user_sgpr_dispatch_id 0
		.amdhsa_user_sgpr_kernarg_preload_length 0
		.amdhsa_user_sgpr_kernarg_preload_offset 0
		.amdhsa_user_sgpr_private_segment_size 0
		.amdhsa_uses_dynamic_stack 0
		.amdhsa_enable_private_segment 0
		.amdhsa_system_sgpr_workgroup_id_x 1
		.amdhsa_system_sgpr_workgroup_id_y 0
		.amdhsa_system_sgpr_workgroup_id_z 0
		.amdhsa_system_sgpr_workgroup_info 0
		.amdhsa_system_vgpr_workitem_id 0
		.amdhsa_next_free_vgpr 256
		.amdhsa_next_free_sgpr 102
		.amdhsa_accum_offset 256
		.amdhsa_reserve_vcc 1
		.amdhsa_float_round_mode_32 0
		.amdhsa_float_round_mode_16_64 0
		.amdhsa_float_denorm_mode_32 3
		.amdhsa_float_denorm_mode_16_64 3
		.amdhsa_dx10_clamp 1
		.amdhsa_ieee_mode 1
		.amdhsa_fp16_overflow 0
		.amdhsa_tg_split 0
		.amdhsa_exception_fp_ieee_invalid_op 0
		.amdhsa_exception_fp_denorm_src 0
		.amdhsa_exception_fp_ieee_div_zero 0
		.amdhsa_exception_fp_ieee_overflow 0
		.amdhsa_exception_fp_ieee_underflow 0
		.amdhsa_exception_fp_ieee_inexact 0
		.amdhsa_exception_int_div_zero 0
	.end_amdhsa_kernel

amdhsa.kernels:
  - .agpr_count:     0
    .args:
      - .offset:         0
        .size:           256
        .value_kind:     by_value
      - .offset:         256
        .size:           4
        .value_kind:     hidden_block_count_x
      - .offset:         260
        .size:           4
        .value_kind:     hidden_block_count_y
      - .offset:         264
        .size:           4
        .value_kind:     hidden_block_count_z
      - .offset:         268
        .size:           2
        .value_kind:     hidden_group_size_x
      - .offset:         270
        .size:           2
        .value_kind:     hidden_group_size_y
      - .offset:         272
        .size:           2
        .value_kind:     hidden_group_size_z
      - .offset:         274
        .size:           2
        .value_kind:     hidden_remainder_x
      - .offset:         276
        .size:           2
        .value_kind:     hidden_remainder_y
      - .offset:         278
        .size:           2
        .value_kind:     hidden_remainder_z
      - .offset:         296
        .size:           8
        .value_kind:     hidden_global_offset_x
      - .offset:         304
        .size:           8
        .value_kind:     hidden_global_offset_y
      - .offset:         312
        .size:           8
        .value_kind:     hidden_global_offset_z
      - .offset:         320
        .size:           2
        .value_kind:     hidden_grid_dims
      - .offset:         376
        .size:           4
        .value_kind:     hidden_dynamic_lds_size
    .group_segment_fixed_size: 0
    .kernarg_segment_align: 8
    .kernarg_segment_size: 512
    .language:       OpenCL C
    .language_version:
      - 2
      - 0
    .max_flat_workgroup_size: 512
    .name:           _Z10fwd_kernel4Args
    .private_segment_fixed_size: 0
    .sgpr_count:     108
    .sgpr_spill_count: 301
    .symbol:         _Z10fwd_kernel4Args.kd
    .uniform_work_group_size: 1
    .uses_dynamic_stack: false
    .vgpr_count:     256
    .vgpr_spill_count: 0
    .wavefront_size: 64
